# baseline (speedup 1.0000x reference)
.LBB1_34:
	s_or_b64 exec, exec, s[0:1]
	s_waitcnt lgkmcnt(0)
	s_barrier
	v_mov_b32_e32 v55, 2
	s_mov_b32 s6, 0xffff
	v_lshlrev_b32_sdwa v35, v55, v32 dst_sel:DWORD dst_unused:UNUSED_PAD src0_sel:DWORD src1_sel:BYTE_0
	v_cvt_f16_f32_sdwa v21, v21 dst_sel:WORD_1 dst_unused:UNUSED_PAD src0_sel:DWORD
	ds_read_b32 v45, v35 offset:10304
	v_lshlrev_b32_sdwa v36, v55, v27 dst_sel:DWORD dst_unused:UNUSED_PAD src0_sel:DWORD src1_sel:BYTE_0
	v_cvt_f16_f32_sdwa v19, v19 dst_sel:WORD_1 dst_unused:UNUSED_PAD src0_sel:DWORD
	ds_read_b32 v46, v36 offset:10304
	v_lshlrev_b32_sdwa v37, v55, v31 dst_sel:DWORD dst_unused:UNUSED_PAD src0_sel:DWORD src1_sel:BYTE_0
	v_cvt_f16_f32_sdwa v17, v17 dst_sel:WORD_1 dst_unused:UNUSED_PAD src0_sel:DWORD
	ds_read_b32 v47, v37 offset:10304
	v_lshlrev_b32_sdwa v38, v55, v26 dst_sel:DWORD dst_unused:UNUSED_PAD src0_sel:DWORD src1_sel:BYTE_0
	v_cvt_f16_f32_sdwa v15, v15 dst_sel:WORD_1 dst_unused:UNUSED_PAD src0_sel:DWORD
	ds_read_b32 v48, v38 offset:10304
	v_lshlrev_b32_sdwa v39, v55, v30 dst_sel:DWORD dst_unused:UNUSED_PAD src0_sel:DWORD src1_sel:BYTE_0
	v_cvt_f16_f32_sdwa v13, v13 dst_sel:WORD_1 dst_unused:UNUSED_PAD src0_sel:DWORD
	ds_read_b32 v49, v39 offset:10304
	v_lshlrev_b32_sdwa v40, v55, v24 dst_sel:DWORD dst_unused:UNUSED_PAD src0_sel:DWORD src1_sel:BYTE_0
	v_cvt_f16_f32_sdwa v11, v11 dst_sel:WORD_1 dst_unused:UNUSED_PAD src0_sel:DWORD
	ds_read_b32 v50, v40 offset:10304
	v_lshlrev_b32_sdwa v41, v55, v29 dst_sel:DWORD dst_unused:UNUSED_PAD src0_sel:DWORD src1_sel:BYTE_0
	v_cvt_f16_f32_sdwa v9, v9 dst_sel:WORD_1 dst_unused:UNUSED_PAD src0_sel:DWORD
	ds_read_b32 v51, v41 offset:10304
	v_lshlrev_b32_sdwa v42, v55, v23 dst_sel:DWORD dst_unused:UNUSED_PAD src0_sel:DWORD src1_sel:BYTE_0
	v_cvt_f16_f32_sdwa v7, v7 dst_sel:WORD_1 dst_unused:UNUSED_PAD src0_sel:DWORD
	ds_read_b32 v52, v42 offset:10304
	v_lshlrev_b32_sdwa v43, v55, v28 dst_sel:DWORD dst_unused:UNUSED_PAD src0_sel:DWORD src1_sel:BYTE_0
	v_cvt_f16_f32_sdwa v5, v5 dst_sel:WORD_1 dst_unused:UNUSED_PAD src0_sel:DWORD
	ds_read_b32 v53, v43 offset:10304
	v_lshlrev_b32_sdwa v44, v55, v22 dst_sel:DWORD dst_unused:UNUSED_PAD src0_sel:DWORD src1_sel:BYTE_0
	v_cvt_f16_f32_sdwa v3, v3 dst_sel:WORD_1 dst_unused:UNUSED_PAD src0_sel:DWORD
	ds_read_b32 v54, v44 offset:10304
	v_and_or_b32 v21, v20, s6, v21
	v_lshrrev_b32_e32 v35, 6, v32
	v_and_or_b32 v19, v18, s6, v19
	v_lshrrev_b32_e32 v36, 6, v27
	v_and_or_b32 v17, v16, s6, v17
	v_lshrrev_b32_e32 v37, 6, v31
	v_and_or_b32 v15, v14, s6, v15
	v_lshrrev_b32_e32 v38, 6, v26
	v_and_or_b32 v13, v12, s6, v13
	v_lshrrev_b32_e32 v39, 6, v30
	v_and_or_b32 v11, v10, s6, v11
	v_lshrrev_b32_e32 v40, 6, v24
	v_and_or_b32 v9, v8, s6, v9
	v_lshrrev_b32_e32 v41, 6, v29
	v_and_or_b32 v7, v6, s6, v7
	v_lshrrev_b32_e32 v42, 6, v23
	v_and_or_b32 v5, v4, s6, v5
	v_lshrrev_b32_e32 v43, 6, v28
	v_and_or_b32 v3, v2, s6, v3
	v_lshrrev_b32_e32 v44, 6, v22
	v_and_b32_e32 v35, 0x3fffffc, v35
	v_and_b32_e32 v36, 0x3fffffc, v36
	v_and_b32_e32 v37, 0x3fffffc, v37
	v_and_b32_e32 v38, 0x3fffffc, v38
	v_and_b32_e32 v39, 0x3fffffc, v39
	v_and_b32_e32 v40, 0x3fffffc, v40
	v_and_b32_e32 v41, 0x3fffffc, v41
	v_and_b32_e32 v42, 0x3fffffc, v42
	v_and_b32_e32 v43, 0x3fffffc, v43
	v_and_b32_e32 v44, 0x3fffffc, v44
	s_waitcnt lgkmcnt(0)
	v_cmp_ne_u32_e32 vcc, -1, v32
	v_lshl_add_u32 v35, v45, 2, v35
	s_and_saveexec_b64 s[0:1], vcc
	ds_write_b32 v35, v21
	s_or_b64 exec, exec, s[0:1]
	v_cmp_ne_u32_e32 vcc, -1, v27
	v_lshl_add_u32 v36, v46, 2, v36
	s_and_saveexec_b64 s[0:1], vcc
	ds_write_b32 v36, v19
	s_or_b64 exec, exec, s[0:1]
	v_cmp_ne_u32_e32 vcc, -1, v31
	v_lshl_add_u32 v37, v47, 2, v37
	s_and_saveexec_b64 s[0:1], vcc
	ds_write_b32 v37, v17
	s_or_b64 exec, exec, s[0:1]
	v_cmp_ne_u32_e32 vcc, -1, v26
	v_lshl_add_u32 v38, v48, 2, v38
	s_and_saveexec_b64 s[0:1], vcc
	ds_write_b32 v38, v15
	s_or_b64 exec, exec, s[0:1]
	v_cmp_ne_u32_e32 vcc, -1, v30
	v_lshl_add_u32 v39, v49, 2, v39
	s_and_saveexec_b64 s[0:1], vcc
	ds_write_b32 v39, v13
	s_or_b64 exec, exec, s[0:1]
	v_cmp_ne_u32_e32 vcc, -1, v24
	v_lshl_add_u32 v40, v50, 2, v40
	s_and_saveexec_b64 s[0:1], vcc
	ds_write_b32 v40, v11
	s_or_b64 exec, exec, s[0:1]
	v_cmp_ne_u32_e32 vcc, -1, v29
	v_lshl_add_u32 v41, v51, 2, v41
	s_and_saveexec_b64 s[0:1], vcc
	ds_write_b32 v41, v9
	s_or_b64 exec, exec, s[0:1]
	v_cmp_ne_u32_e32 vcc, -1, v23
	v_lshl_add_u32 v42, v52, 2, v42
	s_and_saveexec_b64 s[0:1], vcc
	ds_write_b32 v42, v7
	s_or_b64 exec, exec, s[0:1]
	v_cmp_ne_u32_e32 vcc, -1, v28
	v_lshl_add_u32 v43, v53, 2, v43
	s_and_saveexec_b64 s[0:1], vcc
	ds_write_b32 v43, v5
	s_or_b64 exec, exec, s[0:1]
	v_cmp_ne_u32_e32 vcc, -1, v22
	v_lshl_add_u32 v44, v54, 2, v44
	s_and_saveexec_b64 s[0:1], vcc
	ds_write_b32 v44, v3
	s_or_b64 exec, exec, s[0:1]
	s_mov_b64 s[0:1], exec

.LBB1_62:
	s_or_b64 exec, exec, s[10:11]
	v_cmp_lt_i32_e64 s[10:11], v46, v47
	s_and_saveexec_b64 s[30:31], s[10:11]
	s_cbranch_execz .LBB1_49
	s_waitcnt lgkmcnt(0)
	v_lshlrev_b32_e32 v8, 7, v49
	v_and_or_b32 v8, v8, s20, v56
	global_load_dwordx4 v[8:11], v8, s[14:15]
	s_branch .LBB1_49
.LBB1_74:
	s_or_b64 exec, exec, s[28:29]
